# P4 hook gate loads batched (2 waits instead of 8 serialized round trips); final norm and P6 norm: loop-invariant gain loads hoisted out of the row loops
# speedup vs baseline: 1.0080x; 1.0080x over previous
.LBB0_683:
	s_cmpk_lg_i32 s16, 0x800
	s_cbranch_scc1 .LBB0_682
	v_mov_b32_e32 v128, 0
	s_nop 0
	v_add_u32_e32 v128, v128, v178
	v_add_u32_e32 v220, 0x0, v128
	v_mad_i64_i32 v[218:219], s[18:19], v220, s84, v[180:181]
	global_load_dwordx4 v[182:185], v[218:219], off
	global_load_dwordx4 v[202:205], v[218:219], off offset:2048
	v_add_u32_e32 v220, 0x10, v128
	v_mad_i64_i32 v[218:219], s[18:19], v220, s84, v[180:181]
	global_load_dwordx4 v[186:189], v[218:219], off
	global_load_dwordx4 v[206:209], v[218:219], off offset:2048
	v_add_u32_e32 v220, 0x20, v128
	v_mad_i64_i32 v[218:219], s[18:19], v220, s84, v[180:181]
	global_load_dwordx4 v[190:193], v[218:219], off
	global_load_dwordx4 v[210:213], v[218:219], off offset:2048
	v_add_u32_e32 v220, 0x30, v128
	v_mad_i64_i32 v[218:219], s[18:19], v220, s84, v[180:181]
	global_load_dwordx4 v[194:197], v[218:219], off
	global_load_dwordx4 v[214:217], v[218:219], off offset:2048
	s_waitcnt vmcnt(0)
	v_mov_b64_e32 v[130:131], v[182:183]
	v_mov_b64_e32 v[132:133], v[184:185]
	v_mov_b64_e32 v[140:141], v[202:203]
	v_mov_b64_e32 v[142:143], v[204:205]
	v_add_u32_e32 v220, 0x80, v128
	v_mad_i64_i32 v[218:219], s[18:19], v220, s84, v[180:181]
	global_load_dwordx4 v[182:185], v[218:219], off
	global_load_dwordx4 v[202:205], v[218:219], off offset:2048
	v_cvt_f32_ubyte1_e32 v153, v130
	v_cvt_f32_ubyte0_e32 v129, v140
	v_rcp_iflag_f32_e32 v134, v129
	v_cvt_f32_ubyte0_e32 v129, v141
	v_rcp_iflag_f32_e32 v144, v129
	v_cvt_f32_ubyte1_e32 v129, v140
	v_rcp_iflag_f32_e32 v135, v129
	v_cvt_f32_ubyte1_e32 v129, v141
	v_rcp_iflag_f32_e32 v145, v129
	v_cvt_f32_ubyte2_e32 v129, v140
	v_rcp_iflag_f32_e32 v146, v129
	v_cvt_f32_ubyte2_e32 v129, v141
	v_rcp_iflag_f32_e32 v148, v129
	v_cvt_f32_ubyte3_e32 v129, v140
	v_rcp_iflag_f32_e32 v147, v129
	v_cvt_f32_ubyte3_e32 v129, v141
	v_rcp_iflag_f32_e32 v149, v129
	v_cvt_f32_ubyte0_e32 v152, v130
	v_pk_mul_f32 v[134:135], v[134:135], v[152:153]
	v_cvt_f32_ubyte1_e32 v141, v131
	v_cvt_f32_ubyte0_e32 v140, v131
	v_cvt_f32_ubyte3_e32 v151, v130
	v_cvt_f32_ubyte2_e32 v150, v130
	v_pk_mul_f32 v[124:125], v[124:125], v[134:135]
	v_cvt_f32_ubyte3_e32 v135, v131
	v_cvt_f32_ubyte2_e32 v134, v131
	v_pk_mul_f32 v[130:131], v[144:145], v[140:141]
	v_cvt_f32_ubyte0_e32 v129, v142
	v_pk_mul_f32 v[134:135], v[148:149], v[134:135]
	v_pk_mul_f32 v[120:121], v[120:121], v[130:131]
	v_rcp_iflag_f32_e32 v130, v129
	v_cvt_f32_ubyte0_e32 v129, v143
	v_pk_mul_f32 v[122:123], v[122:123], v[134:135]
	v_rcp_iflag_f32_e32 v134, v129
	v_cvt_f32_ubyte1_e32 v129, v142
	v_rcp_iflag_f32_e32 v131, v129
	v_cvt_f32_ubyte1_e32 v129, v143
	v_rcp_iflag_f32_e32 v135, v129
	v_cvt_f32_ubyte2_e32 v129, v142
	v_rcp_iflag_f32_e32 v140, v129
	v_cvt_f32_ubyte2_e32 v129, v143
	v_rcp_iflag_f32_e32 v144, v129
	v_cvt_f32_ubyte3_e32 v129, v142
	v_rcp_iflag_f32_e32 v141, v129
	v_cvt_f32_ubyte3_e32 v129, v143
	v_pk_mul_f32 v[146:147], v[146:147], v[150:151]
	v_rcp_iflag_f32_e32 v145, v129
	v_pk_mul_f32 v[126:127], v[126:127], v[146:147]
	v_cvt_f32_ubyte3_e32 v147, v132
	v_cvt_f32_ubyte2_e32 v146, v132
	v_cvt_f32_ubyte1_e32 v149, v132
	v_cvt_f32_ubyte0_e32 v148, v132
	v_pk_mul_f32 v[130:131], v[130:131], v[148:149]
	v_pk_mul_f32 v[140:141], v[140:141], v[146:147]
	v_pk_mul_f32 v[116:117], v[116:117], v[130:131]
	v_pk_mul_f32 v[118:119], v[118:119], v[140:141]
	v_cvt_f32_ubyte3_e32 v131, v133
	v_cvt_f32_ubyte2_e32 v130, v133
	v_cvt_f32_ubyte1_e32 v141, v133
	v_cvt_f32_ubyte0_e32 v140, v133
	v_pk_mul_f32 v[132:133], v[134:135], v[140:141]
	v_pk_mul_f32 v[130:131], v[144:145], v[130:131]
	v_pk_mul_f32 v[114:115], v[114:115], v[130:131]
	v_pk_mul_f32 v[112:113], v[112:113], v[132:133]
	v_mov_b64_e32 v[130:131], v[186:187]
	v_mov_b64_e32 v[132:133], v[188:189]
	v_mov_b64_e32 v[140:141], v[206:207]
	v_mov_b64_e32 v[142:143], v[208:209]
	v_add_u32_e32 v220, 0x90, v128
	v_mad_i64_i32 v[218:219], s[18:19], v220, s84, v[180:181]
	global_load_dwordx4 v[186:189], v[218:219], off
	global_load_dwordx4 v[206:209], v[218:219], off offset:2048
	v_cvt_f32_ubyte1_e32 v153, v130
	v_cvt_f32_ubyte0_e32 v129, v140
	v_rcp_iflag_f32_e32 v134, v129
	v_cvt_f32_ubyte0_e32 v129, v141
	v_rcp_iflag_f32_e32 v144, v129
	v_cvt_f32_ubyte1_e32 v129, v140
	v_rcp_iflag_f32_e32 v135, v129
	v_cvt_f32_ubyte1_e32 v129, v141
	v_rcp_iflag_f32_e32 v145, v129
	v_cvt_f32_ubyte2_e32 v129, v140
	v_rcp_iflag_f32_e32 v146, v129
	v_cvt_f32_ubyte2_e32 v129, v141
	v_rcp_iflag_f32_e32 v148, v129
	v_cvt_f32_ubyte3_e32 v129, v140
	v_rcp_iflag_f32_e32 v147, v129
	v_cvt_f32_ubyte3_e32 v129, v141
	v_rcp_iflag_f32_e32 v149, v129
	v_cvt_f32_ubyte0_e32 v152, v130
	v_pk_mul_f32 v[134:135], v[134:135], v[152:153]
	v_cvt_f32_ubyte1_e32 v141, v131
	v_cvt_f32_ubyte0_e32 v140, v131
	v_cvt_f32_ubyte3_e32 v151, v130
	v_cvt_f32_ubyte2_e32 v150, v130
	v_pk_mul_f32 v[108:109], v[108:109], v[134:135]
	v_cvt_f32_ubyte3_e32 v135, v131
	v_cvt_f32_ubyte2_e32 v134, v131
	v_pk_mul_f32 v[130:131], v[144:145], v[140:141]
	v_cvt_f32_ubyte0_e32 v129, v142
	v_pk_mul_f32 v[134:135], v[148:149], v[134:135]
	v_pk_mul_f32 v[104:105], v[104:105], v[130:131]
	v_rcp_iflag_f32_e32 v130, v129
	v_cvt_f32_ubyte0_e32 v129, v143
	v_pk_mul_f32 v[106:107], v[106:107], v[134:135]
	v_rcp_iflag_f32_e32 v134, v129
	v_cvt_f32_ubyte1_e32 v129, v142
	v_rcp_iflag_f32_e32 v131, v129
	v_cvt_f32_ubyte1_e32 v129, v143
	v_rcp_iflag_f32_e32 v135, v129
	v_cvt_f32_ubyte2_e32 v129, v142
	v_rcp_iflag_f32_e32 v140, v129
	v_cvt_f32_ubyte2_e32 v129, v143
	v_rcp_iflag_f32_e32 v144, v129
	v_cvt_f32_ubyte3_e32 v129, v142
	v_rcp_iflag_f32_e32 v141, v129
	v_cvt_f32_ubyte3_e32 v129, v143
	v_pk_mul_f32 v[146:147], v[146:147], v[150:151]
	v_rcp_iflag_f32_e32 v145, v129
	v_pk_mul_f32 v[110:111], v[110:111], v[146:147]
	v_cvt_f32_ubyte3_e32 v147, v132
	v_cvt_f32_ubyte2_e32 v146, v132
	v_cvt_f32_ubyte1_e32 v149, v132
	v_cvt_f32_ubyte0_e32 v148, v132
	v_pk_mul_f32 v[130:131], v[130:131], v[148:149]
	v_pk_mul_f32 v[140:141], v[140:141], v[146:147]
	v_pk_mul_f32 v[100:101], v[100:101], v[130:131]
	v_pk_mul_f32 v[102:103], v[102:103], v[140:141]
	v_cvt_f32_ubyte3_e32 v131, v133
	v_cvt_f32_ubyte2_e32 v130, v133
	v_cvt_f32_ubyte1_e32 v141, v133
	v_cvt_f32_ubyte0_e32 v140, v133
	v_pk_mul_f32 v[132:133], v[134:135], v[140:141]
	v_pk_mul_f32 v[130:131], v[144:145], v[130:131]
	v_pk_mul_f32 v[98:99], v[98:99], v[130:131]
	v_pk_mul_f32 v[96:97], v[96:97], v[132:133]
	v_mov_b64_e32 v[130:131], v[190:191]
	v_mov_b64_e32 v[132:133], v[192:193]
	v_mov_b64_e32 v[140:141], v[210:211]
	v_mov_b64_e32 v[142:143], v[212:213]
	v_add_u32_e32 v220, 0xa0, v128
	v_mad_i64_i32 v[218:219], s[18:19], v220, s84, v[180:181]
	global_load_dwordx4 v[190:193], v[218:219], off
	global_load_dwordx4 v[210:213], v[218:219], off offset:2048
	v_cvt_f32_ubyte1_e32 v153, v130
	v_cvt_f32_ubyte0_e32 v129, v140
	v_rcp_iflag_f32_e32 v134, v129
	v_cvt_f32_ubyte0_e32 v129, v141
	v_rcp_iflag_f32_e32 v144, v129
	v_cvt_f32_ubyte1_e32 v129, v140
	v_rcp_iflag_f32_e32 v135, v129
	v_cvt_f32_ubyte1_e32 v129, v141
	v_rcp_iflag_f32_e32 v145, v129
	v_cvt_f32_ubyte2_e32 v129, v140
	v_rcp_iflag_f32_e32 v146, v129
	v_cvt_f32_ubyte2_e32 v129, v141
	v_rcp_iflag_f32_e32 v148, v129
	v_cvt_f32_ubyte3_e32 v129, v140
	v_rcp_iflag_f32_e32 v147, v129
	v_cvt_f32_ubyte3_e32 v129, v141
	v_rcp_iflag_f32_e32 v149, v129
	v_cvt_f32_ubyte0_e32 v152, v130
	v_pk_mul_f32 v[134:135], v[134:135], v[152:153]
	v_cvt_f32_ubyte1_e32 v141, v131
	v_cvt_f32_ubyte0_e32 v140, v131
	v_cvt_f32_ubyte3_e32 v151, v130
	v_cvt_f32_ubyte2_e32 v150, v130
	v_pk_mul_f32 v[92:93], v[92:93], v[134:135]
	v_cvt_f32_ubyte3_e32 v135, v131
	v_cvt_f32_ubyte2_e32 v134, v131
	v_pk_mul_f32 v[130:131], v[144:145], v[140:141]
	v_cvt_f32_ubyte0_e32 v129, v142
	v_pk_mul_f32 v[134:135], v[148:149], v[134:135]
	v_pk_mul_f32 v[88:89], v[88:89], v[130:131]
	v_rcp_iflag_f32_e32 v130, v129
	v_cvt_f32_ubyte0_e32 v129, v143
	v_pk_mul_f32 v[90:91], v[90:91], v[134:135]
	v_rcp_iflag_f32_e32 v134, v129
	v_cvt_f32_ubyte1_e32 v129, v142
	v_rcp_iflag_f32_e32 v131, v129
	v_cvt_f32_ubyte1_e32 v129, v143
	v_rcp_iflag_f32_e32 v135, v129
	v_cvt_f32_ubyte2_e32 v129, v142
	v_rcp_iflag_f32_e32 v140, v129
	v_cvt_f32_ubyte2_e32 v129, v143
	v_rcp_iflag_f32_e32 v144, v129
	v_cvt_f32_ubyte3_e32 v129, v142
	v_rcp_iflag_f32_e32 v141, v129
	v_cvt_f32_ubyte3_e32 v129, v143
	v_pk_mul_f32 v[146:147], v[146:147], v[150:151]
	v_rcp_iflag_f32_e32 v145, v129
	v_pk_mul_f32 v[94:95], v[94:95], v[146:147]
	v_cvt_f32_ubyte3_e32 v147, v132
	v_cvt_f32_ubyte2_e32 v146, v132
	v_cvt_f32_ubyte1_e32 v149, v132
	v_cvt_f32_ubyte0_e32 v148, v132
	v_pk_mul_f32 v[130:131], v[130:131], v[148:149]
	v_pk_mul_f32 v[140:141], v[140:141], v[146:147]
	v_pk_mul_f32 v[84:85], v[84:85], v[130:131]
	v_pk_mul_f32 v[86:87], v[86:87], v[140:141]
	v_cvt_f32_ubyte3_e32 v131, v133
	v_cvt_f32_ubyte2_e32 v130, v133
	v_cvt_f32_ubyte1_e32 v141, v133
	v_cvt_f32_ubyte0_e32 v140, v133
	v_pk_mul_f32 v[132:133], v[134:135], v[140:141]
	v_pk_mul_f32 v[130:131], v[144:145], v[130:131]
	v_pk_mul_f32 v[82:83], v[82:83], v[130:131]
	v_pk_mul_f32 v[80:81], v[80:81], v[132:133]
	v_mov_b64_e32 v[130:131], v[194:195]
	v_mov_b64_e32 v[132:133], v[196:197]
	v_mov_b64_e32 v[140:141], v[214:215]
	v_mov_b64_e32 v[142:143], v[216:217]
	v_add_u32_e32 v220, 0xb0, v128
	v_mad_i64_i32 v[218:219], s[18:19], v220, s84, v[180:181]
	global_load_dwordx4 v[194:197], v[218:219], off
	global_load_dwordx4 v[214:217], v[218:219], off offset:2048
	v_cvt_f32_ubyte1_e32 v153, v130
	v_cvt_f32_ubyte0_e32 v129, v140
	v_rcp_iflag_f32_e32 v134, v129
	v_cvt_f32_ubyte0_e32 v129, v141
	v_rcp_iflag_f32_e32 v144, v129
	v_cvt_f32_ubyte1_e32 v129, v140
	v_rcp_iflag_f32_e32 v135, v129
	v_cvt_f32_ubyte1_e32 v129, v141
	v_rcp_iflag_f32_e32 v145, v129
	v_cvt_f32_ubyte2_e32 v129, v140
	v_rcp_iflag_f32_e32 v146, v129
	v_cvt_f32_ubyte2_e32 v129, v141
	v_rcp_iflag_f32_e32 v148, v129
	v_cvt_f32_ubyte3_e32 v129, v140
	v_rcp_iflag_f32_e32 v147, v129
	v_cvt_f32_ubyte3_e32 v129, v141
	v_rcp_iflag_f32_e32 v149, v129
	v_cvt_f32_ubyte0_e32 v152, v130
	v_pk_mul_f32 v[134:135], v[134:135], v[152:153]
	v_cvt_f32_ubyte1_e32 v141, v131
	v_cvt_f32_ubyte0_e32 v140, v131
	v_cvt_f32_ubyte3_e32 v151, v130
	v_cvt_f32_ubyte2_e32 v150, v130
	v_pk_mul_f32 v[76:77], v[76:77], v[134:135]
	v_cvt_f32_ubyte3_e32 v135, v131
	v_cvt_f32_ubyte2_e32 v134, v131
	v_pk_mul_f32 v[130:131], v[144:145], v[140:141]
	v_cvt_f32_ubyte0_e32 v129, v142
	v_pk_mul_f32 v[134:135], v[148:149], v[134:135]
	v_pk_mul_f32 v[72:73], v[72:73], v[130:131]
	v_rcp_iflag_f32_e32 v130, v129
	v_cvt_f32_ubyte0_e32 v129, v143
	v_pk_mul_f32 v[74:75], v[74:75], v[134:135]
	v_rcp_iflag_f32_e32 v134, v129
	v_cvt_f32_ubyte1_e32 v129, v142
	v_rcp_iflag_f32_e32 v131, v129
	v_cvt_f32_ubyte1_e32 v129, v143
	v_rcp_iflag_f32_e32 v135, v129
	v_cvt_f32_ubyte2_e32 v129, v142
	v_rcp_iflag_f32_e32 v140, v129
	v_cvt_f32_ubyte2_e32 v129, v143
	v_rcp_iflag_f32_e32 v144, v129
	v_cvt_f32_ubyte3_e32 v129, v142
	v_rcp_iflag_f32_e32 v141, v129
	v_cvt_f32_ubyte3_e32 v129, v143
	v_pk_mul_f32 v[146:147], v[146:147], v[150:151]
	v_rcp_iflag_f32_e32 v145, v129
	v_pk_mul_f32 v[78:79], v[78:79], v[146:147]
	v_cvt_f32_ubyte3_e32 v147, v132
	v_cvt_f32_ubyte2_e32 v146, v132
	v_cvt_f32_ubyte1_e32 v149, v132
	v_cvt_f32_ubyte0_e32 v148, v132
	v_pk_mul_f32 v[130:131], v[130:131], v[148:149]
	v_pk_mul_f32 v[140:141], v[140:141], v[146:147]
	v_pk_mul_f32 v[68:69], v[68:69], v[130:131]
	v_pk_mul_f32 v[70:71], v[70:71], v[140:141]
	v_cvt_f32_ubyte3_e32 v131, v133
	v_cvt_f32_ubyte2_e32 v130, v133
	v_cvt_f32_ubyte1_e32 v141, v133
	v_cvt_f32_ubyte0_e32 v140, v133
	v_pk_mul_f32 v[132:133], v[134:135], v[140:141]
	v_pk_mul_f32 v[130:131], v[144:145], v[130:131]
	v_pk_mul_f32 v[66:67], v[66:67], v[130:131]
	v_pk_mul_f32 v[64:65], v[64:65], v[132:133]
	s_waitcnt vmcnt(0)
	v_mov_b64_e32 v[130:131], v[182:183]
	v_mov_b64_e32 v[132:133], v[184:185]
	v_mov_b64_e32 v[140:141], v[202:203]
	v_mov_b64_e32 v[142:143], v[204:205]
	v_cvt_f32_ubyte1_e32 v153, v130
	v_cvt_f32_ubyte0_e32 v129, v140
	v_rcp_iflag_f32_e32 v134, v129
	v_cvt_f32_ubyte0_e32 v129, v141
	v_rcp_iflag_f32_e32 v144, v129
	v_cvt_f32_ubyte1_e32 v129, v140
	v_rcp_iflag_f32_e32 v135, v129
	v_cvt_f32_ubyte1_e32 v129, v141
	v_rcp_iflag_f32_e32 v145, v129
	v_cvt_f32_ubyte2_e32 v129, v140
	v_rcp_iflag_f32_e32 v146, v129
	v_cvt_f32_ubyte2_e32 v129, v141
	v_rcp_iflag_f32_e32 v148, v129
	v_cvt_f32_ubyte3_e32 v129, v140
	v_rcp_iflag_f32_e32 v147, v129
	v_cvt_f32_ubyte3_e32 v129, v141
	v_rcp_iflag_f32_e32 v149, v129
	v_cvt_f32_ubyte0_e32 v152, v130
	v_pk_mul_f32 v[134:135], v[134:135], v[152:153]
	v_cvt_f32_ubyte1_e32 v141, v131
	v_cvt_f32_ubyte0_e32 v140, v131
	v_cvt_f32_ubyte3_e32 v151, v130
	v_cvt_f32_ubyte2_e32 v150, v130
	v_pk_mul_f32 v[60:61], v[60:61], v[134:135]
	v_cvt_f32_ubyte3_e32 v135, v131
	v_cvt_f32_ubyte2_e32 v134, v131
	v_pk_mul_f32 v[130:131], v[144:145], v[140:141]
	v_cvt_f32_ubyte0_e32 v129, v142
	v_pk_mul_f32 v[134:135], v[148:149], v[134:135]
	v_pk_mul_f32 v[56:57], v[56:57], v[130:131]
	v_rcp_iflag_f32_e32 v130, v129
	v_cvt_f32_ubyte0_e32 v129, v143
	v_pk_mul_f32 v[58:59], v[58:59], v[134:135]
	v_rcp_iflag_f32_e32 v134, v129
	v_cvt_f32_ubyte1_e32 v129, v142
	v_rcp_iflag_f32_e32 v131, v129
	v_cvt_f32_ubyte1_e32 v129, v143
	v_rcp_iflag_f32_e32 v135, v129
	v_cvt_f32_ubyte2_e32 v129, v142
	v_rcp_iflag_f32_e32 v140, v129
	v_cvt_f32_ubyte2_e32 v129, v143
	v_rcp_iflag_f32_e32 v144, v129
	v_cvt_f32_ubyte3_e32 v129, v142
	v_rcp_iflag_f32_e32 v141, v129
	v_cvt_f32_ubyte3_e32 v129, v143
	v_pk_mul_f32 v[146:147], v[146:147], v[150:151]
	v_rcp_iflag_f32_e32 v145, v129
	v_pk_mul_f32 v[62:63], v[62:63], v[146:147]
	v_cvt_f32_ubyte3_e32 v147, v132
	v_cvt_f32_ubyte2_e32 v146, v132
	v_cvt_f32_ubyte1_e32 v149, v132
	v_cvt_f32_ubyte0_e32 v148, v132
	v_pk_mul_f32 v[130:131], v[130:131], v[148:149]
	v_pk_mul_f32 v[140:141], v[140:141], v[146:147]
	v_pk_mul_f32 v[52:53], v[52:53], v[130:131]
	v_pk_mul_f32 v[54:55], v[54:55], v[140:141]
	v_cvt_f32_ubyte3_e32 v131, v133
	v_cvt_f32_ubyte2_e32 v130, v133
	v_cvt_f32_ubyte1_e32 v141, v133
	v_cvt_f32_ubyte0_e32 v140, v133
	v_pk_mul_f32 v[132:133], v[134:135], v[140:141]
	v_pk_mul_f32 v[130:131], v[144:145], v[130:131]
	v_pk_mul_f32 v[50:51], v[50:51], v[130:131]
	v_pk_mul_f32 v[48:49], v[48:49], v[132:133]
	v_mov_b64_e32 v[130:131], v[186:187]
	v_mov_b64_e32 v[132:133], v[188:189]
	v_mov_b64_e32 v[140:141], v[206:207]
	v_mov_b64_e32 v[142:143], v[208:209]
	v_cvt_f32_ubyte1_e32 v153, v130
	v_cvt_f32_ubyte0_e32 v129, v140
	v_rcp_iflag_f32_e32 v134, v129
	v_cvt_f32_ubyte0_e32 v129, v141
	v_rcp_iflag_f32_e32 v144, v129
	v_cvt_f32_ubyte1_e32 v129, v140
	v_rcp_iflag_f32_e32 v135, v129
	v_cvt_f32_ubyte1_e32 v129, v141
	v_rcp_iflag_f32_e32 v145, v129
	v_cvt_f32_ubyte2_e32 v129, v140
	v_rcp_iflag_f32_e32 v146, v129
	v_cvt_f32_ubyte2_e32 v129, v141
	v_rcp_iflag_f32_e32 v148, v129
	v_cvt_f32_ubyte3_e32 v129, v140
	v_rcp_iflag_f32_e32 v147, v129
	v_cvt_f32_ubyte3_e32 v129, v141
	v_rcp_iflag_f32_e32 v149, v129
	v_cvt_f32_ubyte0_e32 v152, v130
	v_pk_mul_f32 v[134:135], v[134:135], v[152:153]
	v_cvt_f32_ubyte1_e32 v141, v131
	v_cvt_f32_ubyte0_e32 v140, v131
	v_cvt_f32_ubyte3_e32 v151, v130
	v_cvt_f32_ubyte2_e32 v150, v130
	v_pk_mul_f32 v[44:45], v[44:45], v[134:135]
	v_cvt_f32_ubyte3_e32 v135, v131
	v_cvt_f32_ubyte2_e32 v134, v131
	v_pk_mul_f32 v[130:131], v[144:145], v[140:141]
	v_cvt_f32_ubyte0_e32 v129, v142
	v_pk_mul_f32 v[134:135], v[148:149], v[134:135]
	v_pk_mul_f32 v[40:41], v[40:41], v[130:131]
	v_rcp_iflag_f32_e32 v130, v129
	v_cvt_f32_ubyte0_e32 v129, v143
	v_pk_mul_f32 v[42:43], v[42:43], v[134:135]
	v_rcp_iflag_f32_e32 v134, v129
	v_cvt_f32_ubyte1_e32 v129, v142
	v_rcp_iflag_f32_e32 v131, v129
	v_cvt_f32_ubyte1_e32 v129, v143
	v_rcp_iflag_f32_e32 v135, v129
	v_cvt_f32_ubyte2_e32 v129, v142
	v_rcp_iflag_f32_e32 v140, v129
	v_cvt_f32_ubyte2_e32 v129, v143
	v_rcp_iflag_f32_e32 v144, v129
	v_cvt_f32_ubyte3_e32 v129, v142
	v_rcp_iflag_f32_e32 v141, v129
	v_cvt_f32_ubyte3_e32 v129, v143
	v_pk_mul_f32 v[146:147], v[146:147], v[150:151]
	v_rcp_iflag_f32_e32 v145, v129
	v_pk_mul_f32 v[46:47], v[46:47], v[146:147]
	v_cvt_f32_ubyte3_e32 v147, v132
	v_cvt_f32_ubyte2_e32 v146, v132
	v_cvt_f32_ubyte1_e32 v149, v132
	v_cvt_f32_ubyte0_e32 v148, v132
	v_pk_mul_f32 v[130:131], v[130:131], v[148:149]
	v_pk_mul_f32 v[140:141], v[140:141], v[146:147]
	v_pk_mul_f32 v[36:37], v[36:37], v[130:131]
	v_pk_mul_f32 v[38:39], v[38:39], v[140:141]
	v_cvt_f32_ubyte3_e32 v131, v133
	v_cvt_f32_ubyte2_e32 v130, v133
	v_cvt_f32_ubyte1_e32 v141, v133
	v_cvt_f32_ubyte0_e32 v140, v133
	v_pk_mul_f32 v[132:133], v[134:135], v[140:141]
	v_pk_mul_f32 v[130:131], v[144:145], v[130:131]
	v_pk_mul_f32 v[34:35], v[34:35], v[130:131]
	v_pk_mul_f32 v[32:33], v[32:33], v[132:133]
	v_mov_b64_e32 v[130:131], v[190:191]
	v_mov_b64_e32 v[132:133], v[192:193]
	v_mov_b64_e32 v[140:141], v[210:211]
	v_mov_b64_e32 v[142:143], v[212:213]
	v_cvt_f32_ubyte1_e32 v153, v130
	v_cvt_f32_ubyte0_e32 v129, v140
	v_rcp_iflag_f32_e32 v134, v129
	v_cvt_f32_ubyte0_e32 v129, v141
	v_rcp_iflag_f32_e32 v144, v129
	v_cvt_f32_ubyte1_e32 v129, v140
	v_rcp_iflag_f32_e32 v135, v129
	v_cvt_f32_ubyte1_e32 v129, v141
	v_rcp_iflag_f32_e32 v145, v129
	v_cvt_f32_ubyte2_e32 v129, v140
	v_rcp_iflag_f32_e32 v146, v129
	v_cvt_f32_ubyte2_e32 v129, v141
	v_rcp_iflag_f32_e32 v148, v129
	v_cvt_f32_ubyte3_e32 v129, v140
	v_rcp_iflag_f32_e32 v147, v129
	v_cvt_f32_ubyte3_e32 v129, v141
	v_rcp_iflag_f32_e32 v149, v129
	v_cvt_f32_ubyte0_e32 v152, v130
	v_pk_mul_f32 v[134:135], v[134:135], v[152:153]
	v_cvt_f32_ubyte1_e32 v141, v131
	v_cvt_f32_ubyte0_e32 v140, v131
	v_cvt_f32_ubyte3_e32 v151, v130
	v_cvt_f32_ubyte2_e32 v150, v130
	v_pk_mul_f32 v[28:29], v[28:29], v[134:135]
	v_cvt_f32_ubyte3_e32 v135, v131
	v_cvt_f32_ubyte2_e32 v134, v131
	v_pk_mul_f32 v[130:131], v[144:145], v[140:141]
	v_cvt_f32_ubyte0_e32 v129, v142
	v_pk_mul_f32 v[134:135], v[148:149], v[134:135]
	v_pk_mul_f32 v[24:25], v[24:25], v[130:131]
	v_rcp_iflag_f32_e32 v130, v129
	v_cvt_f32_ubyte0_e32 v129, v143
	v_pk_mul_f32 v[26:27], v[26:27], v[134:135]
	v_rcp_iflag_f32_e32 v134, v129
	v_cvt_f32_ubyte1_e32 v129, v142
	v_rcp_iflag_f32_e32 v131, v129
	v_cvt_f32_ubyte1_e32 v129, v143
	v_rcp_iflag_f32_e32 v135, v129
	v_cvt_f32_ubyte2_e32 v129, v142
	v_rcp_iflag_f32_e32 v140, v129
	v_cvt_f32_ubyte2_e32 v129, v143
	v_rcp_iflag_f32_e32 v144, v129
	v_cvt_f32_ubyte3_e32 v129, v142
	v_rcp_iflag_f32_e32 v141, v129
	v_pk_mul_f32 v[146:147], v[146:147], v[150:151]
	v_cvt_f32_ubyte3_e32 v129, v143
	v_pk_mul_f32 v[30:31], v[30:31], v[146:147]
	v_cvt_f32_ubyte3_e32 v147, v132
	v_cvt_f32_ubyte2_e32 v146, v132
	v_rcp_iflag_f32_e32 v145, v129
	v_cvt_f32_ubyte1_e32 v149, v132
	v_cvt_f32_ubyte0_e32 v148, v132
	v_pk_mul_f32 v[140:141], v[140:141], v[146:147]
	v_pk_mul_f32 v[130:131], v[130:131], v[148:149]
	v_pk_mul_f32 v[22:23], v[22:23], v[140:141]
	v_cvt_f32_ubyte1_e32 v141, v133
	v_cvt_f32_ubyte0_e32 v140, v133
	v_pk_mul_f32 v[20:21], v[20:21], v[130:131]
	v_cvt_f32_ubyte3_e32 v131, v133
	v_cvt_f32_ubyte2_e32 v130, v133
	v_pk_mul_f32 v[132:133], v[134:135], v[140:141]
	v_pk_mul_f32 v[130:131], v[144:145], v[130:131]
	v_pk_mul_f32 v[16:17], v[16:17], v[132:133]
	v_pk_mul_f32 v[18:19], v[18:19], v[130:131]
	v_mov_b64_e32 v[128:129], v[194:195]
	v_mov_b64_e32 v[130:131], v[196:197]
	v_mov_b64_e32 v[132:133], v[214:215]
	v_mov_b64_e32 v[134:135], v[216:217]
	v_cvt_f32_ubyte3_e32 v149, v128
	v_cvt_f32_ubyte0_e32 v141, v133
	v_cvt_f32_ubyte0_e32 v140, v132
	v_rcp_iflag_f32_e32 v142, v141
	v_cvt_f32_ubyte1_e32 v141, v132
	v_rcp_iflag_f32_e32 v140, v140
	v_rcp_iflag_f32_e32 v141, v141
	v_cvt_f32_ubyte1_e32 v143, v133
	v_rcp_iflag_f32_e32 v143, v143
	v_cvt_f32_ubyte2_e32 v145, v133
	v_cvt_f32_ubyte2_e32 v148, v128
	v_cvt_f32_ubyte1_e32 v151, v128
	v_cvt_f32_ubyte0_e32 v150, v128
	v_cvt_f32_ubyte3_e32 v128, v133
	v_rcp_iflag_f32_e32 v146, v145
	v_rcp_iflag_f32_e32 v147, v128
	v_pk_mul_f32 v[140:141], v[140:141], v[150:151]
	v_cvt_f32_ubyte2_e32 v144, v132
	v_cvt_f32_ubyte3_e32 v132, v132
	v_pk_mul_f32 v[12:13], v[12:13], v[140:141]
	v_cvt_f32_ubyte1_e32 v141, v129
	v_cvt_f32_ubyte0_e32 v140, v129
	v_rcp_iflag_f32_e32 v145, v132
	v_cvt_f32_ubyte3_e32 v133, v129
	v_cvt_f32_ubyte2_e32 v132, v129
	v_pk_mul_f32 v[128:129], v[142:143], v[140:141]
	v_pk_mul_f32 v[132:133], v[146:147], v[132:133]
	v_pk_mul_f32 v[8:9], v[8:9], v[128:129]
	v_cvt_f32_ubyte0_e32 v129, v135
	v_pk_mul_f32 v[10:11], v[10:11], v[132:133]
	v_cvt_f32_ubyte0_e32 v128, v134
	v_rcp_iflag_f32_e32 v132, v129
	v_cvt_f32_ubyte1_e32 v129, v134
	v_rcp_iflag_f32_e32 v128, v128
	v_rcp_iflag_f32_e32 v129, v129
	v_cvt_f32_ubyte1_e32 v147, v130
	v_cvt_f32_ubyte0_e32 v146, v130
	v_rcp_iflag_f32_e32 v144, v144
	v_pk_mul_f32 v[128:129], v[128:129], v[146:147]
	v_cvt_f32_ubyte1_e32 v133, v135
	v_cvt_f32_ubyte2_e32 v140, v134
	v_cvt_f32_ubyte2_e32 v141, v135
	v_cvt_f32_ubyte3_e32 v134, v134
	v_pk_mul_f32 v[4:5], v[4:5], v[128:129]
	v_cvt_f32_ubyte3_e32 v128, v135
	v_rcp_iflag_f32_e32 v133, v133
	v_rcp_iflag_f32_e32 v140, v140
	v_rcp_iflag_f32_e32 v142, v141
	v_rcp_iflag_f32_e32 v141, v134
	v_rcp_iflag_f32_e32 v143, v128
	v_pk_mul_f32 v[144:145], v[144:145], v[148:149]
	v_cvt_f32_ubyte3_e32 v129, v131
	v_pk_mul_f32 v[14:15], v[14:15], v[144:145]
	v_cvt_f32_ubyte3_e32 v145, v130
	v_cvt_f32_ubyte2_e32 v144, v130
	v_cvt_f32_ubyte2_e32 v128, v131
	v_cvt_f32_ubyte1_e32 v135, v131
	v_cvt_f32_ubyte0_e32 v134, v131
	v_pk_mul_f32 v[140:141], v[140:141], v[144:145]
	v_pk_mul_f32 v[130:131], v[132:133], v[134:135]
	v_pk_mul_f32 v[128:129], v[142:143], v[128:129]
	v_pk_mul_f32 v[6:7], v[6:7], v[140:141]
	v_pk_mul_f32 v[2:3], v[2:3], v[128:129]
	v_pk_mul_f32 v[0:1], v[0:1], v[130:131]
	s_branch .LBB0_682

.LBB0_800:
	s_or_b64 exec, exec, s[0:1]
	s_mov_b32 s2, s71
	s_waitcnt lgkmcnt(0)
	s_barrier
	v_mbcnt_lo_u32_b32 v0, -1, 0
	v_mbcnt_hi_u32_b32 v0, -1, v0
	s_add_i32 s1, s2, 0
	v_add_u32_e32 v1, s67, v0
	s_add_i32 s4, s1, 0x26b78
	v_readfirstlane_b32 s0, v1
	v_mov_b32_e32 v1, s4
	s_add_i32 s4, s1, 0x26b7c
	v_mov_b32_e32 v2, s4
	s_add_i32 s4, s1, 0x26b48
	s_add_i32 s1, s1, 0x26b4c
	v_mov_b32_e32 v3, s4
	v_mov_b32_e32 v4, s1
	ds_read_b32 v1, v1
	ds_read_b32 v2, v2
	ds_read_b32 v3, v3
	ds_read_b32 v4, v4
	s_ashr_i32 s3, s0, 6
	s_add_i32 s0, s2, s66
	s_lshl_b32 s1, s0, 3
	s_add_i32 s12, s1, s3
	s_waitcnt lgkmcnt(0)
	v_readfirstlane_b32 s13, v2
	v_readfirstlane_b32 s14, v1
	v_readfirstlane_b32 s0, v4
	s_cmp_lt_i32 s12, 0x8000
	v_readfirstlane_b32 s4, v3
	s_mov_b32 s15, 0xffff0000
	s_mov_b64 s[16:17], 0x15a00000
	s_mov_b64 s[18:19], 0x9a00000
	s_mov_b32 s20, 0x15a00000
	s_mov_b32 s21, 0x9a00000
	s_cbranch_scc0 .LBB0_803
	v_readlane_b32 s6, v255, 6
	v_readlane_b32 s7, v255, 7
	s_add_i32 s8, s2, s64
	s_lshl_b64 s[6:7], s[6:7], 13
	s_add_u32 s4, s4, s6
	v_and_b32_e32 v0, 63, v0
	s_addc_u32 s5, s0, s7
	v_lshlrev_b32_e32 v160, 5, v0
	v_lshl_add_u64 v[8:9], s[4:5], 0, v[160:161]
	s_mov_b64 s[4:5], 0x1000
	v_lshl_add_u64 v[10:11], v[8:9], 0, s[4:5]
	s_mov_b64 s[4:5], 0x1800
	v_lshl_add_u64 v[12:13], v[8:9], 0, s[4:5]
	s_lshl_b32 s0, s8, 4
	s_ashr_i32 s5, s3, 31
	s_ashr_i32 s6, s1, 31
	s_add_u32 s4, s3, s1
	s_addc_u32 s5, s5, s6
	s_ashr_i32 s1, s0, 31
	s_lshl_b64 s[8:9], s[0:1], 12
	v_readlane_b32 s1, v255, 4
	s_add_i32 s1, s1, s3
	s_lshl_b32 s2, s2, 4
	s_add_i32 s2, s1, s2
	s_ashr_i32 s3, s2, 31
	s_lshl_b64 s[6:7], s[4:5], 12
	s_lshl_b64 s[10:11], s[2:3], 12
	v_lshlrev_b32_e32 v160, 4, v0
	global_load_dwordx4 v[136:139], v[8:9], off offset:16
	global_load_dwordx4 v[140:143], v[8:9], off
	global_load_dwordx4 v[144:147], v[8:9], off offset:2048
	global_load_dwordx4 v[148:151], v[8:9], off offset:2064
	global_load_dwordx4 v[152:155], v[10:11], off
	global_load_dwordx4 v[156:159], v[10:11], off offset:16
	global_load_dwordx4 v[164:167], v[12:13], off
	global_load_dwordx4 v[168:171], v[12:13], off offset:16
	s_waitcnt vmcnt(0)
.LBB0_802:
	s_add_u32 s2, s14, s6
	s_addc_u32 s3, s13, s7
	s_add_u32 s4, s14, s10
	v_lshl_add_u64 v[16:17], s[2:3], 0, v[160:161]
	s_addc_u32 s5, s13, s11
	v_add_co_u32_e32 v20, vcc, s20, v16
	v_lshl_add_u64 v[18:19], v[16:17], 0, s[16:17]
	v_lshl_add_u64 v[34:35], s[4:5], 0, v[160:161]
	v_addc_co_u32_e32 v21, vcc, 0, v17, vcc
	global_load_dwordx4 v[22:25], v[18:19], off offset:1024 nt
	global_load_dwordx4 v[26:29], v[18:19], off offset:2048 nt
	global_load_dwordx4 v[30:33], v[20:21], off nt
	v_add_co_u32_e32 v20, vcc, s20, v34
	v_lshl_add_u64 v[44:45], v[34:35], 0, s[16:17]
	s_nop 0
	v_addc_co_u32_e32 v21, vcc, 0, v35, vcc
	global_load_dwordx4 v[40:43], v[44:45], off offset:1024 nt
	global_load_dwordx4 v[64:67], v[44:45], off offset:2048 nt
	global_load_dwordx4 v[68:71], v[18:19], off offset:3072 nt
	global_load_dwordx4 v[72:75], v[44:45], off offset:3072 nt
	global_load_dwordx4 v[76:79], v[20:21], off nt
	v_add_co_u32_e64 v36, s[2:3], s21, v16
	v_lshl_add_u64 v[14:15], v[16:17], 0, s[18:19]
	s_nop 0
	v_addc_co_u32_e64 v37, s[2:3], 0, v17, s[2:3]
	v_add_co_u32_e64 v38, s[2:3], s21, v34
	v_lshl_add_u64 v[16:17], v[34:35], 0, s[18:19]
	s_nop 0
	v_addc_co_u32_e64 v39, s[2:3], 0, v35, s[2:3]
	s_add_i32 s12, s12, s0
	s_add_u32 s14, s14, s8
	s_addc_u32 s13, s13, s9
	s_cmpk_gt_i32 s12, 0x7fff
	s_waitcnt vmcnt(0)
	v_cvt_f32_f16_e32 v84, v22
	v_cvt_f32_f16_sdwa v85, v22 dst_sel:DWORD dst_unused:UNUSED_PAD src0_sel:WORD_1
	v_cvt_f32_f16_e32 v86, v23
	v_cvt_f32_f16_sdwa v87, v23 dst_sel:DWORD dst_unused:UNUSED_PAD src0_sel:WORD_1
	v_cvt_f32_f16_e32 v80, v24
	v_cvt_f32_f16_sdwa v81, v24 dst_sel:DWORD dst_unused:UNUSED_PAD src0_sel:WORD_1
	v_cvt_f32_f16_e32 v82, v25
	v_cvt_f32_f16_sdwa v83, v25 dst_sel:DWORD dst_unused:UNUSED_PAD src0_sel:WORD_1
	v_cvt_f32_f16_e32 v60, v26
	v_cvt_f32_f16_sdwa v61, v26 dst_sel:DWORD dst_unused:UNUSED_PAD src0_sel:WORD_1
	v_cvt_f32_f16_e32 v62, v27
	v_cvt_f32_f16_sdwa v63, v27 dst_sel:DWORD dst_unused:UNUSED_PAD src0_sel:WORD_1
	v_cvt_f32_f16_e32 v56, v28
	v_cvt_f32_f16_sdwa v57, v28 dst_sel:DWORD dst_unused:UNUSED_PAD src0_sel:WORD_1
	v_cvt_f32_f16_e32 v58, v29
	v_cvt_f32_f16_sdwa v59, v29 dst_sel:DWORD dst_unused:UNUSED_PAD src0_sel:WORD_1
	v_cvt_f32_f16_e32 v90, v30
	v_cvt_f32_f16_sdwa v91, v30 dst_sel:DWORD dst_unused:UNUSED_PAD src0_sel:WORD_1
	v_cvt_f32_f16_e32 v92, v31
	v_cvt_f32_f16_sdwa v93, v31 dst_sel:DWORD dst_unused:UNUSED_PAD src0_sel:WORD_1
	v_cvt_f32_f16_e32 v94, v32
	v_cvt_f32_f16_sdwa v95, v32 dst_sel:DWORD dst_unused:UNUSED_PAD src0_sel:WORD_1
	v_cvt_f32_f16_e32 v96, v33
	v_cvt_f32_f16_sdwa v97, v33 dst_sel:DWORD dst_unused:UNUSED_PAD src0_sel:WORD_1
	v_cvt_f32_f16_e32 v48, v40
	v_cvt_f32_f16_sdwa v49, v40 dst_sel:DWORD dst_unused:UNUSED_PAD src0_sel:WORD_1
	v_cvt_f32_f16_e32 v50, v41
	v_cvt_f32_f16_sdwa v51, v41 dst_sel:DWORD dst_unused:UNUSED_PAD src0_sel:WORD_1
	v_cvt_f32_f16_e32 v52, v42
	v_cvt_f32_f16_sdwa v53, v42 dst_sel:DWORD dst_unused:UNUSED_PAD src0_sel:WORD_1
	v_cvt_f32_f16_e32 v54, v43
	v_cvt_f32_f16_sdwa v55, v43 dst_sel:DWORD dst_unused:UNUSED_PAD src0_sel:WORD_1
	v_cvt_f32_f16_e32 v44, v64
	v_cvt_f32_f16_sdwa v45, v64 dst_sel:DWORD dst_unused:UNUSED_PAD src0_sel:WORD_1
	v_cvt_f32_f16_e32 v46, v65
	v_cvt_f32_f16_sdwa v47, v65 dst_sel:DWORD dst_unused:UNUSED_PAD src0_sel:WORD_1
	v_cvt_f32_f16_e32 v40, v66
	v_cvt_f32_f16_sdwa v41, v66 dst_sel:DWORD dst_unused:UNUSED_PAD src0_sel:WORD_1
	v_cvt_f32_f16_e32 v42, v67
	v_cvt_f32_f16_sdwa v43, v67 dst_sel:DWORD dst_unused:UNUSED_PAD src0_sel:WORD_1
	v_cvt_f32_f16_e32 v18, v68
	v_cvt_f32_f16_sdwa v19, v68 dst_sel:DWORD dst_unused:UNUSED_PAD src0_sel:WORD_1
	v_cvt_f32_f16_e32 v20, v69
	v_cvt_f32_f16_sdwa v21, v69 dst_sel:DWORD dst_unused:UNUSED_PAD src0_sel:WORD_1
	v_cvt_f32_f16_e32 v22, v70
	v_cvt_f32_f16_sdwa v23, v70 dst_sel:DWORD dst_unused:UNUSED_PAD src0_sel:WORD_1
	v_cvt_f32_f16_e32 v24, v71
	v_cvt_f32_f16_sdwa v25, v71 dst_sel:DWORD dst_unused:UNUSED_PAD src0_sel:WORD_1
	v_cvt_f32_f16_e32 v26, v72
	v_cvt_f32_f16_sdwa v27, v72 dst_sel:DWORD dst_unused:UNUSED_PAD src0_sel:WORD_1
	v_cvt_f32_f16_e32 v28, v73
	v_cvt_f32_f16_sdwa v29, v73 dst_sel:DWORD dst_unused:UNUSED_PAD src0_sel:WORD_1
	v_cvt_f32_f16_e32 v30, v74
	v_cvt_f32_f16_sdwa v31, v74 dst_sel:DWORD dst_unused:UNUSED_PAD src0_sel:WORD_1
	v_cvt_f32_f16_e32 v32, v75
	v_cvt_f32_f16_sdwa v33, v75 dst_sel:DWORD dst_unused:UNUSED_PAD src0_sel:WORD_1
	v_cvt_f32_f16_e32 v64, v76
	v_cvt_f32_f16_sdwa v65, v76 dst_sel:DWORD dst_unused:UNUSED_PAD src0_sel:WORD_1
	v_cvt_f32_f16_e32 v66, v77
	v_cvt_f32_f16_sdwa v67, v77 dst_sel:DWORD dst_unused:UNUSED_PAD src0_sel:WORD_1
	v_cvt_f32_f16_e32 v68, v78
	v_cvt_f32_f16_sdwa v69, v78 dst_sel:DWORD dst_unused:UNUSED_PAD src0_sel:WORD_1
	v_cvt_f32_f16_e32 v70, v79
	v_cvt_f32_f16_sdwa v71, v79 dst_sel:DWORD dst_unused:UNUSED_PAD src0_sel:WORD_1
	v_pk_mul_f32 v[34:35], v[84:85], v[84:85]
	v_pk_mul_f32 v[72:73], v[86:87], v[86:87]
	v_pk_mul_f32 v[74:75], v[80:81], v[80:81]
	v_pk_mul_f32 v[76:77], v[82:83], v[82:83]
	v_pk_mul_f32 v[78:79], v[60:61], v[60:61]
	v_pk_mul_f32 v[88:89], v[62:63], v[62:63]
	v_pk_mul_f32 v[98:99], v[56:57], v[56:57]
	v_pk_mul_f32 v[100:101], v[58:59], v[58:59]
	v_pk_mul_f32 v[102:103], v[90:91], v[90:91]
	v_pk_mul_f32 v[104:105], v[92:93], v[92:93]
	v_pk_mul_f32 v[106:107], v[94:95], v[94:95]
	v_pk_mul_f32 v[108:109], v[96:97], v[96:97]
	v_add_f32_e32 v122, v72, v73
	v_add_f32_e32 v123, v34, v35
	v_add_f32_e32 v124, v76, v77
	v_add_f32_e32 v125, v74, v75
	v_add_f32_e32 v126, v88, v89
	v_add_f32_e32 v127, v78, v79
	v_add_f32_e32 v128, v100, v101
	v_add_f32_e32 v129, v98, v99
	v_add_f32_e32 v130, v108, v109
	v_add_f32_e32 v131, v106, v107
	v_add_f32_e32 v132, v104, v105
	v_add_f32_e32 v133, v102, v103
	v_pk_mul_f32 v[34:35], v[48:49], v[48:49]
	v_pk_mul_f32 v[72:73], v[50:51], v[50:51]
	v_pk_mul_f32 v[74:75], v[52:53], v[52:53]
	v_pk_mul_f32 v[76:77], v[54:55], v[54:55]
	v_pk_mul_f32 v[78:79], v[44:45], v[44:45]
	v_pk_mul_f32 v[88:89], v[46:47], v[46:47]
	v_pk_mul_f32 v[98:99], v[40:41], v[40:41]
	v_pk_mul_f32 v[100:101], v[42:43], v[42:43]
	v_pk_mul_f32 v[114:115], v[26:27], v[26:27]
	v_pk_mul_f32 v[116:117], v[28:29], v[28:29]
	v_add_f32_e32 v134, v123, v122
	v_add_f32_e32 v135, v125, v124
	v_add_f32_e32 v126, v127, v126
	v_add_f32_e32 v127, v129, v128
	v_pk_mul_f32 v[102:103], v[30:31], v[30:31]
	v_pk_mul_f32 v[104:105], v[32:33], v[32:33]
	v_pk_mul_f32 v[106:107], v[64:65], v[64:65]
	v_pk_mul_f32 v[108:109], v[66:67], v[66:67]
	v_pk_mul_f32 v[122:123], v[68:69], v[68:69]
	v_pk_mul_f32 v[124:125], v[70:71], v[70:71]
	v_add_f32_e32 v128, v131, v130
	v_add_f32_e32 v129, v133, v132
	v_add_f32_e32 v72, v72, v73
	v_add_f32_e32 v34, v34, v35
	v_add_f32_e32 v35, v76, v77
	v_add_f32_e32 v73, v74, v75
	v_add_f32_e32 v74, v88, v89
	v_add_f32_e32 v75, v78, v79
	v_add_f32_e32 v76, v100, v101
	v_add_f32_e32 v77, v98, v99
	v_add_f32_e32 v78, v116, v117
	v_add_f32_e32 v79, v114, v115
	v_add_f32_e32 v88, v104, v105
	v_add_f32_e32 v89, v102, v103
	v_add_f32_e32 v98, v129, v128
	v_add_f32_e32 v101, v124, v125
	v_add_f32_e32 v102, v122, v123
	v_add_f32_e32 v103, v108, v109
	v_add_f32_e32 v104, v106, v107
	v_add_f32_e32 v34, v34, v72
	v_add_f32_e32 v35, v73, v35
	v_add_f32_e32 v72, v75, v74
	v_add_f32_e32 v73, v77, v76
	v_add_f32_e32 v74, v79, v78
	v_add_f32_e32 v76, v98, v134
	v_add_f32_e32 v77, v102, v101
	v_add_f32_e32 v78, v104, v103
	v_pk_mul_f32 v[110:111], v[18:19], v[18:19]
	v_pk_mul_f32 v[112:113], v[20:21], v[20:21]
	v_add_f32_e32 v76, v135, v76
	v_add_f32_e32 v77, v78, v77
	v_pk_mul_f32 v[118:119], v[22:23], v[22:23]
	v_pk_mul_f32 v[120:121], v[24:25], v[24:25]
	v_add_f32_e32 v112, v112, v113
	v_add_f32_e32 v110, v110, v111
	v_add_f32_e32 v76, v76, v126
	v_add_f32_e32 v34, v77, v34
	v_add_f32_e32 v111, v120, v121
	v_add_f32_e32 v113, v118, v119
	v_add_f32_e32 v99, v110, v112
	v_add_f32_e32 v76, v127, v76
	v_add_f32_e32 v34, v35, v34
	v_add_f32_e32 v100, v113, v111
	v_add_f32_e32 v35, v76, v99
	v_add_f32_e32 v34, v34, v72
	v_add_f32_e32 v35, v100, v35
	v_add_f32_e32 v34, v73, v34
	v_add_f32_e32 v75, v89, v88
	v_add_f32_e32 v34, v34, v74
	ds_swizzle_b32 v72, v35 offset:swizzle(SWAP,1)
	v_add_f32_e32 v34, v75, v34
	ds_swizzle_b32 v73, v34 offset:swizzle(SWAP,1)
	s_waitcnt lgkmcnt(1)
	v_add_f32_e32 v35, v35, v72
	ds_swizzle_b32 v72, v35 offset:swizzle(SWAP,2)
	s_waitcnt lgkmcnt(1)
	v_add_f32_e32 v34, v34, v73
	ds_swizzle_b32 v73, v34 offset:swizzle(SWAP,2)
	s_waitcnt lgkmcnt(1)
	v_add_f32_e32 v35, v35, v72
	ds_swizzle_b32 v72, v35 offset:swizzle(SWAP,4)
	s_waitcnt lgkmcnt(1)
	v_add_f32_e32 v34, v34, v73
	ds_swizzle_b32 v73, v34 offset:swizzle(SWAP,4)
	s_waitcnt lgkmcnt(1)
	v_add_f32_e32 v35, v35, v72
	ds_swizzle_b32 v72, v35 offset:swizzle(SWAP,8)
	s_waitcnt lgkmcnt(1)
	v_add_f32_e32 v34, v34, v73
	ds_swizzle_b32 v73, v34 offset:swizzle(SWAP,8)
	s_waitcnt lgkmcnt(1)
	v_add_f32_e32 v35, v35, v72
	ds_swizzle_b32 v72, v35 offset:swizzle(SWAP,16)
	s_waitcnt lgkmcnt(1)
	v_add_f32_e32 v34, v34, v73
	ds_swizzle_b32 v73, v34 offset:swizzle(SWAP,16)
	s_waitcnt lgkmcnt(1)
	v_add_f32_e32 v35, v35, v72
	v_mov_b32_e32 v72, v35
	s_waitcnt lgkmcnt(0)
	v_add_f32_e32 v34, v34, v73
	v_permlane32_swap_b32_e32 v35, v72
	v_add_f32_e32 v35, v35, v72
	v_mov_b32_e32 v72, v34
	s_nop 1
	v_permlane32_swap_b32_e32 v34, v72
	v_fmamk_f32 v35, v35, 0x3a000000, v254
	v_add_f32_e32 v34, v34, v72
	v_mul_f32_e32 v72, 0x4f800000, v35
	v_cmp_gt_f32_e32 vcc, s76, v35
	v_fmamk_f32 v34, v34, 0x3a000000, v254
	v_mul_f32_e32 v73, 0x4f800000, v34
	v_cndmask_b32_e32 v35, v35, v72, vcc
	v_sqrt_f32_e32 v72, v35
	v_cmp_gt_f32_e64 s[2:3], s76, v34
	v_add_u32_e32 v74, -1, v72
	s_nop 0
	v_cndmask_b32_e64 v34, v34, v73, s[2:3]
	v_sqrt_f32_e32 v73, v34
	v_add_u32_e32 v75, 1, v72
	v_fma_f32 v76, -v74, v72, v35
	v_fma_f32 v77, -v75, v72, v35
	v_cmp_ge_f32_e64 s[4:5], 0, v76
	v_add_u32_e32 v76, 1, v73
	s_nop 0
	v_cndmask_b32_e64 v72, v72, v74, s[4:5]
	v_add_u32_e32 v74, -1, v73
	v_cmp_lt_f32_e64 s[4:5], 0, v77
	v_fma_f32 v77, -v76, v73, v34
	s_nop 0
	v_cndmask_b32_e64 v72, v72, v75, s[4:5]
	v_fma_f32 v75, -v74, v73, v34
	v_cmp_ge_f32_e64 s[4:5], 0, v75
	v_mul_f32_e32 v78, 0x37800000, v72
	v_cndmask_b32_e32 v72, v72, v78, vcc
	v_cndmask_b32_e64 v73, v73, v74, s[4:5]
	v_cmp_lt_f32_e64 s[4:5], 0, v77
	v_cmp_class_f32_e32 vcc, v35, v229
	s_nop 0
	v_cndmask_b32_e64 v73, v73, v76, s[4:5]
	v_cndmask_b32_e32 v72, v72, v35, vcc
	v_mul_f32_e32 v35, 0x37800000, v73
	v_div_scale_f32 v74, s[4:5], v72, v72, 1.0
	v_cndmask_b32_e64 v35, v73, v35, s[2:3]
	v_cmp_class_f32_e64 s[2:3], v34, v229
	v_rcp_f32_e32 v73, v74
	v_div_scale_f32 v75, vcc, 1.0, v72, 1.0
	v_cndmask_b32_e64 v35, v35, v34, s[2:3]
	v_div_scale_f32 v76, s[2:3], v35, v35, 1.0
	v_rcp_f32_e32 v78, v76
	v_fma_f32 v34, -v74, v73, 1.0
	v_fmac_f32_e32 v73, v34, v73
	v_mul_f32_e32 v34, v75, v73
	v_fma_f32 v79, -v76, v78, 1.0
	v_div_scale_f32 v77, s[2:3], 1.0, v35, 1.0
	v_fma_f32 v88, -v74, v34, v75
	v_fmac_f32_e32 v78, v79, v78
	v_fmac_f32_e32 v34, v88, v73
	v_mul_f32_e32 v79, v77, v78
	v_fma_f32 v74, -v74, v34, v75
	v_fma_f32 v75, -v76, v79, v77
	v_div_fmas_f32 v34, v74, v73, v34
	v_fmac_f32_e32 v79, v75, v78
	v_div_fixup_f32 v34, v34, v72, 1.0
	v_fma_f32 v72, -v76, v79, v77
	s_mov_b64 vcc, s[2:3]
	v_div_fmas_f32 v88, v72, v78, v79
	v_pk_mul_f32 v[72:73], v[90:91], v[34:35] op_sel_hi:[1,0]
	v_pk_mul_f32 v[76:77], v[92:93], v[34:35] op_sel_hi:[1,0]
	v_pk_mul_f32 v[74:75], v[94:95], v[34:35] op_sel_hi:[1,0]
	v_pk_mul_f32 v[78:79], v[96:97], v[34:35] op_sel_hi:[1,0]
	v_pk_mul_f32 v[90:91], v[56:57], v[34:35] op_sel_hi:[1,0]
	v_div_fixup_f32 v56, v88, v35, 1.0
	v_pk_mul_f32 v[76:77], v[142:143], v[76:77]
	v_pk_mul_f32 v[72:73], v[140:141], v[72:73]
	v_pk_mul_f32 v[74:75], v[136:137], v[74:75]
	v_pk_mul_f32 v[84:85], v[84:85], v[34:35] op_sel_hi:[1,0]
	v_pk_mul_f32 v[86:87], v[86:87], v[34:35] op_sel_hi:[1,0]
	v_pk_mul_f32 v[80:81], v[80:81], v[34:35] op_sel_hi:[1,0]
	v_pk_mul_f32 v[82:83], v[82:83], v[34:35] op_sel_hi:[1,0]
	v_pk_mul_f32 v[60:61], v[60:61], v[34:35] op_sel_hi:[1,0]
	v_pk_mul_f32 v[62:63], v[62:63], v[34:35] op_sel_hi:[1,0]
	v_pk_mul_f32 v[58:59], v[58:59], v[34:35] op_sel_hi:[1,0]
	v_pk_mul_f32 v[78:79], v[138:139], v[78:79]
	v_pk_mul_f32 v[64:65], v[64:65], v[56:57] op_sel_hi:[1,0]
	v_pk_mul_f32 v[66:67], v[66:67], v[56:57] op_sel_hi:[1,0]
	v_pk_mul_f32 v[68:69], v[68:69], v[56:57] op_sel_hi:[1,0]
	v_pk_mul_f32 v[70:71], v[70:71], v[56:57] op_sel_hi:[1,0]
	v_bfe_u32 v35, v72, 16, 1
	v_bfe_u32 v57, v73, 16, 1
	v_bfe_u32 v94, v76, 16, 1
	v_bfe_u32 v96, v74, 16, 1
	v_bfe_u32 v95, v77, 16, 1
	v_bfe_u32 v97, v75, 16, 1
	v_bfe_u32 v98, v78, 16, 1
	v_pk_mul_f32 v[88:89], v[44:45], v[56:57] op_sel_hi:[1,0]
	v_pk_mul_f32 v[92:93], v[46:47], v[56:57] op_sel_hi:[1,0]
	v_pk_mul_f32 v[44:45], v[40:41], v[56:57] op_sel_hi:[1,0]
	v_pk_mul_f32 v[46:47], v[42:43], v[56:57] op_sel_hi:[1,0]
	v_pk_mul_f32 v[6:7], v[142:143], v[66:67]
	v_pk_mul_f32 v[4:5], v[140:141], v[64:65]
	v_pk_mul_f32 v[40:41], v[138:139], v[70:71]
	v_pk_mul_f32 v[42:43], v[136:137], v[68:69]
	v_add3_u32 v0, v72, v35, s75
	v_add3_u32 v2, v76, v94, s75
	v_add3_u32 v35, v74, v96, s75
	v_bfe_u32 v99, v79, 16, 1
	v_pk_mul_f32 v[48:49], v[48:49], v[56:57] op_sel_hi:[1,0]
	v_pk_mul_f32 v[50:51], v[50:51], v[56:57] op_sel_hi:[1,0]
	v_pk_mul_f32 v[52:53], v[52:53], v[56:57] op_sel_hi:[1,0]
	v_pk_mul_f32 v[54:55], v[54:55], v[56:57] op_sel_hi:[1,0]
	v_add3_u32 v1, v73, v57, s75
	v_add3_u32 v3, v77, v95, s75
	v_add3_u32 v57, v75, v97, s75
	v_add3_u32 v64, v78, v98, s75
	v_lshrrev_b32_e32 v0, 16, v0
	v_lshrrev_b32_e32 v2, 16, v2
	v_lshrrev_b32_e32 v35, 16, v35
	v_bfe_u32 v66, v4, 16, 1
	v_bfe_u32 v68, v6, 16, 1
	v_bfe_u32 v70, v42, 16, 1
	v_bfe_u32 v72, v40, 16, 1
	v_add3_u32 v65, v79, v99, s75
	v_lshrrev_b32_e32 v64, 16, v64
	v_bfe_u32 v67, v5, 16, 1
	v_bfe_u32 v69, v7, 16, 1
	v_bfe_u32 v71, v43, 16, 1
	v_bfe_u32 v73, v41, 16, 1
	v_and_or_b32 v0, v1, s15, v0
	v_and_or_b32 v1, v3, s15, v2
	v_and_or_b32 v2, v57, s15, v35
	v_add3_u32 v4, v4, v66, s75
	v_add3_u32 v6, v6, v68, s75
	v_add3_u32 v35, v42, v70, s75
	v_add3_u32 v40, v40, v72, s75
	v_and_or_b32 v3, v65, s15, v64
	v_add3_u32 v5, v5, v67, s75
	v_add3_u32 v7, v7, v69, s75
	v_add3_u32 v42, v43, v71, s75
	v_add3_u32 v41, v41, v73, s75
	v_lshrrev_b32_e32 v4, 16, v4
	v_lshrrev_b32_e32 v6, 16, v6
	v_lshrrev_b32_e32 v35, 16, v35
	v_lshrrev_b32_e32 v40, 16, v40
	global_store_dwordx4 v[36:37], v[0:3], off
	s_nop 1
	v_and_or_b32 v0, v5, s15, v4
	v_and_or_b32 v1, v7, s15, v6
	v_and_or_b32 v2, v42, s15, v35
	v_and_or_b32 v3, v41, s15, v40
	global_store_dwordx4 v[38:39], v[0:3], off
	s_nop 0
	v_pk_mul_f32 v[36:37], v[146:147], v[86:87]
	v_pk_mul_f32 v[38:39], v[144:145], v[84:85]
	v_pk_mul_f32 v[40:41], v[150:151], v[82:83]
	v_pk_mul_f32 v[42:43], v[148:149], v[80:81]
	v_pk_mul_f32 v[2:3], v[146:147], v[50:51]
	v_pk_mul_f32 v[0:1], v[144:145], v[48:49]
	v_pk_mul_f32 v[6:7], v[150:151], v[54:55]
	v_pk_mul_f32 v[4:5], v[148:149], v[52:53]
	v_bfe_u32 v35, v38, 16, 1
	v_bfe_u32 v48, v39, 16, 1
	v_bfe_u32 v49, v36, 16, 1
	v_bfe_u32 v51, v42, 16, 1
	v_bfe_u32 v53, v40, 16, 1
	v_bfe_u32 v50, v37, 16, 1
	v_bfe_u32 v52, v43, 16, 1
	v_bfe_u32 v54, v41, 16, 1
	v_bfe_u32 v55, v0, 16, 1
	v_bfe_u32 v57, v1, 16, 1
	v_bfe_u32 v64, v2, 16, 1
	v_bfe_u32 v65, v3, 16, 1
	v_bfe_u32 v66, v4, 16, 1
	v_bfe_u32 v67, v5, 16, 1
	v_bfe_u32 v68, v6, 16, 1
	v_add3_u32 v35, v38, v35, s75
	v_add3_u32 v38, v39, v48, s75
	v_add3_u32 v36, v36, v49, s75
	v_add3_u32 v39, v42, v51, s75
	v_add3_u32 v40, v40, v53, s75
	v_bfe_u32 v69, v7, 16, 1
	v_add3_u32 v37, v37, v50, s75
	v_add3_u32 v42, v43, v52, s75
	v_add3_u32 v41, v41, v54, s75
	v_add3_u32 v0, v0, v55, s75
	v_add3_u32 v43, v1, v57, s75
	v_add3_u32 v1, v2, v64, s75
	v_add3_u32 v48, v3, v65, s75
	v_add3_u32 v2, v4, v66, s75
	v_add3_u32 v49, v5, v67, s75
	v_add3_u32 v3, v6, v68, s75
	v_lshrrev_b32_e32 v4, 16, v35
	v_lshrrev_b32_e32 v5, 16, v36
	v_lshrrev_b32_e32 v6, 16, v39
	v_lshrrev_b32_e32 v35, 16, v40
	v_add3_u32 v7, v7, v69, s75
	v_lshrrev_b32_e32 v36, 16, v0
	v_lshrrev_b32_e32 v39, 16, v1
	v_lshrrev_b32_e32 v40, 16, v2
	v_lshrrev_b32_e32 v50, 16, v3
	v_and_or_b32 v0, v38, s15, v4
	v_and_or_b32 v1, v37, s15, v5
	v_and_or_b32 v2, v42, s15, v6
	v_and_or_b32 v3, v41, s15, v35
	v_and_or_b32 v4, v43, s15, v36
	v_and_or_b32 v5, v48, s15, v39
	v_and_or_b32 v6, v49, s15, v40
	v_and_or_b32 v7, v7, s15, v50
	global_store_dwordx4 v[14:15], v[0:3], off offset:1024
	global_store_dwordx4 v[16:17], v[4:7], off offset:1024
	s_nop 0
	v_pk_mul_f32 v[38:39], v[154:155], v[62:63]
	v_pk_mul_f32 v[42:43], v[152:153], v[60:61]
	v_pk_mul_f32 v[6:7], v[58:59], v[158:159]
	v_pk_mul_f32 v[40:41], v[90:91], v[156:157]
	v_pk_mul_f32 v[4:5], v[154:155], v[92:93]
	v_pk_mul_f32 v[36:37], v[152:153], v[88:89]
	v_pk_mul_f32 v[2:3], v[158:159], v[46:47]
	v_pk_mul_f32 v[0:1], v[156:157], v[44:45]
	v_bfe_u32 v35, v42, 16, 1
	v_bfe_u32 v45, v38, 16, 1
	v_bfe_u32 v47, v40, 16, 1
	v_bfe_u32 v49, v6, 16, 1
	v_bfe_u32 v44, v43, 16, 1
	v_bfe_u32 v46, v39, 16, 1
	v_bfe_u32 v48, v41, 16, 1
	v_bfe_u32 v50, v7, 16, 1
	v_bfe_u32 v51, v36, 16, 1
	v_bfe_u32 v53, v4, 16, 1
	v_bfe_u32 v55, v0, 16, 1
	v_bfe_u32 v57, v1, 16, 1
	v_bfe_u32 v58, v2, 16, 1
	v_bfe_u32 v59, v3, 16, 1
	v_add3_u32 v35, v42, v35, s75
	v_add3_u32 v38, v38, v45, s75
	v_add3_u32 v40, v40, v47, s75
	v_add3_u32 v6, v6, v49, s75
	v_bfe_u32 v52, v37, 16, 1
	v_bfe_u32 v54, v5, 16, 1
	v_add3_u32 v42, v43, v44, s75
	v_add3_u32 v39, v39, v46, s75
	v_add3_u32 v41, v41, v48, s75
	v_add3_u32 v7, v7, v50, s75
	v_add3_u32 v36, v36, v51, s75
	v_add3_u32 v4, v4, v53, s75
	v_add3_u32 v0, v0, v55, s75
	v_add3_u32 v43, v1, v57, s75
	v_add3_u32 v1, v2, v58, s75
	v_add3_u32 v44, v3, v59, s75
	v_lshrrev_b32_e32 v2, 16, v35
	v_lshrrev_b32_e32 v3, 16, v38
	v_lshrrev_b32_e32 v35, 16, v40
	v_lshrrev_b32_e32 v6, 16, v6
	v_add3_u32 v37, v37, v52, s75
	v_add3_u32 v5, v5, v54, s75
	v_lshrrev_b32_e32 v36, 16, v36
	v_lshrrev_b32_e32 v38, 16, v4
	v_lshrrev_b32_e32 v40, 16, v0
	v_lshrrev_b32_e32 v45, 16, v1
	v_and_or_b32 v0, v42, s15, v2
	v_and_or_b32 v1, v39, s15, v3
	v_and_or_b32 v2, v41, s15, v35
	v_and_or_b32 v3, v7, s15, v6
	v_and_or_b32 v4, v37, s15, v36
	v_and_or_b32 v5, v5, s15, v38
	v_and_or_b32 v6, v43, s15, v40
	v_and_or_b32 v7, v44, s15, v45
	global_store_dwordx4 v[14:15], v[0:3], off offset:2048
	global_store_dwordx4 v[16:17], v[4:7], off offset:2048
	s_nop 0
	v_pk_mul_f32 v[18:19], v[18:19], v[34:35] op_sel_hi:[1,0]
	v_pk_mul_f32 v[20:21], v[20:21], v[34:35] op_sel_hi:[1,0]
	v_pk_mul_f32 v[22:23], v[22:23], v[34:35] op_sel_hi:[1,0]
	v_pk_mul_f32 v[24:25], v[24:25], v[34:35] op_sel_hi:[1,0]
	v_pk_mul_f32 v[26:27], v[26:27], v[56:57] op_sel_hi:[1,0]
	v_pk_mul_f32 v[28:29], v[28:29], v[56:57] op_sel_hi:[1,0]
	v_pk_mul_f32 v[30:31], v[30:31], v[56:57] op_sel_hi:[1,0]
	v_pk_mul_f32 v[32:33], v[32:33], v[56:57] op_sel_hi:[1,0]
	v_pk_mul_f32 v[20:21], v[20:21], v[166:167]
	v_pk_mul_f32 v[18:19], v[18:19], v[164:165]
	v_pk_mul_f32 v[24:25], v[24:25], v[170:171]
	v_pk_mul_f32 v[22:23], v[22:23], v[168:169]
	v_pk_mul_f32 v[6:7], v[28:29], v[166:167]
	v_pk_mul_f32 v[4:5], v[26:27], v[164:165]
	v_pk_mul_f32 v[2:3], v[32:33], v[170:171]
	v_pk_mul_f32 v[0:1], v[30:31], v[168:169]
	v_bfe_u32 v26, v18, 16, 1
	v_bfe_u32 v28, v20, 16, 1
	v_bfe_u32 v30, v22, 16, 1
	v_bfe_u32 v32, v24, 16, 1
	v_bfe_u32 v27, v19, 16, 1
	v_bfe_u32 v29, v21, 16, 1
	v_bfe_u32 v31, v23, 16, 1
	v_bfe_u32 v33, v25, 16, 1
	v_bfe_u32 v34, v4, 16, 1
	v_bfe_u32 v36, v6, 16, 1
	v_bfe_u32 v38, v0, 16, 1
	v_bfe_u32 v39, v1, 16, 1
	v_bfe_u32 v40, v2, 16, 1
	v_bfe_u32 v41, v3, 16, 1
	v_add3_u32 v18, v18, v26, s75
	v_add3_u32 v20, v20, v28, s75
	v_add3_u32 v22, v22, v30, s75
	v_add3_u32 v24, v24, v32, s75
	v_bfe_u32 v35, v5, 16, 1
	v_bfe_u32 v37, v7, 16, 1
	v_add3_u32 v19, v19, v27, s75
	v_add3_u32 v21, v21, v29, s75
	v_add3_u32 v23, v23, v31, s75
	v_add3_u32 v25, v25, v33, s75
	v_add3_u32 v4, v4, v34, s75
	v_add3_u32 v6, v6, v36, s75
	v_add3_u32 v0, v0, v38, s75
	v_add3_u32 v26, v1, v39, s75
	v_add3_u32 v1, v2, v40, s75
	v_add3_u32 v27, v3, v41, s75
	v_lshrrev_b32_e32 v2, 16, v18
	v_lshrrev_b32_e32 v3, 16, v20
	v_lshrrev_b32_e32 v18, 16, v22
	v_lshrrev_b32_e32 v20, 16, v24
	v_add3_u32 v5, v5, v35, s75
	v_add3_u32 v7, v7, v37, s75
	v_lshrrev_b32_e32 v4, 16, v4
	v_lshrrev_b32_e32 v6, 16, v6
	v_lshrrev_b32_e32 v22, 16, v0
	v_lshrrev_b32_e32 v24, 16, v1
	v_and_or_b32 v0, v19, s15, v2
	v_and_or_b32 v1, v21, s15, v3
	v_and_or_b32 v2, v23, s15, v18
	v_and_or_b32 v3, v25, s15, v20
	v_and_or_b32 v4, v5, s15, v4
	v_and_or_b32 v5, v7, s15, v6
	v_and_or_b32 v6, v26, s15, v22
	v_and_or_b32 v7, v27, s15, v24
	global_store_dwordx4 v[14:15], v[0:3], off offset:3072
	global_store_dwordx4 v[16:17], v[4:7], off offset:3072
	s_cbranch_scc0 .LBB0_802

.LBB0_976:
	v_mbcnt_lo_u32_b32 v0, -1, 0
	v_mbcnt_hi_u32_b32 v0, -1, v0
	s_mov_b32 s3, 0
	v_add_u32_e32 v1, s67, v0
	s_add_i32 s1, s3, s66
	v_readfirstlane_b32 s0, v1
	s_ashr_i32 s0, s0, 6
	s_lshl_b32 s1, s1, 3
	s_add_i32 s2, s1, s0
	s_add_i32 s0, s3, 0
	s_add_i32 s1, s0, 0x26b78
	v_mov_b32_e32 v1, s1
	s_add_i32 s1, s0, 0x26b7c
	v_mov_b32_e32 v2, s1
	s_add_i32 s1, s0, 0x26b70
	v_mov_b32_e32 v3, s1
	s_add_i32 s1, s0, 0x26b74
	v_mov_b32_e32 v4, s1
	s_add_i32 s1, s0, 0x26b68
	s_add_i32 s0, s0, 0x26b6c
	v_mov_b32_e32 v5, s1
	v_mov_b32_e32 v6, s0
	ds_read_b32 v1, v1
	ds_read_b32 v2, v2
	ds_read_b32 v3, v3
	ds_read_b32 v4, v4
	ds_read_b32 v5, v5
	ds_read_b32 v6, v6
	s_waitcnt lgkmcnt(0)
	v_readfirstlane_b32 s5, v2
	v_readfirstlane_b32 s6, v1
	v_readfirstlane_b32 s11, v4
	v_readfirstlane_b32 s10, v3
	v_readfirstlane_b32 s1, v6
	s_cmpk_gt_i32 s2, 0x7fff
	v_readfirstlane_b32 s0, v5
	s_cbranch_scc1 .LBB0_979
	v_and_b32_e32 v12, 63, v0
	v_mov_b32_e32 v1, 0
	v_lshlrev_b32_e32 v0, 5, v12
	v_lshl_add_u64 v[2:3], s[0:1], 0, v[0:1]
	s_mov_b64 s[0:1], 0x1000
	v_lshl_add_u64 v[4:5], v[2:3], 0, s[0:1]
	s_mov_b64 s[0:1], 0x1010
	s_add_i32 s3, s3, s64
	v_lshl_add_u64 v[6:7], v[2:3], 0, s[0:1]
	s_mov_b64 s[0:1], 0x1800
	s_lshl_b32 s4, s3, 3
	v_lshl_add_u64 v[8:9], v[2:3], 0, s[0:1]
	s_mov_b64 s[0:1], 0x1810
	s_ashr_i32 s3, s2, 31
	v_lshl_add_u64 v[10:11], v[2:3], 0, s[0:1]
	s_lshl_b64 s[0:1], s[2:3], 12
	s_add_u32 s0, s6, s0
	s_addc_u32 s1, s5, s1
	s_add_u32 s6, s0, 0x15a00000
	s_addc_u32 s7, s1, 0
	s_ashr_i32 s5, s4, 31
	s_lshl_b64 s[8:9], s[4:5], 12
	s_lshl_b64 s[0:1], s[2:3], 13
	v_lshlrev_b32_e32 v14, 1, v12
	s_add_u32 s10, s10, s0
	s_addc_u32 s11, s11, s1
	s_lshl_b64 s[12:13], s[4:5], 13
	v_lshlrev_b32_e32 v12, 4, v12
	v_lshlrev_b32_e32 v0, 4, v14
	v_mov_b32_e32 v13, 0x358637bd
	s_mov_b32 s3, 0xf800000
	v_mov_b32_e32 v14, 0x260
	s_movk_i32 s5, 0x1000
	global_load_dwordx4 v[84:87], v[2:3], off
	global_load_dwordx4 v[88:91], v[2:3], off offset:16
	global_load_dwordx4 v[92:95], v[2:3], off offset:2048
	global_load_dwordx4 v[96:99], v[2:3], off offset:2064
	global_load_dwordx4 v[100:103], v[4:5], off
	global_load_dwordx4 v[104:107], v[6:7], off
	global_load_dwordx4 v[108:111], v[8:9], off
	global_load_dwordx4 v[112:115], v[10:11], off
	s_waitcnt vmcnt(0)
.LBB0_978:
	global_load_dwordx4 v[16:19], v12, s[6:7] nt
	global_load_dwordx4 v[20:23], v12, s[6:7] offset:1024 nt
	global_load_dwordx4 v[24:27], v12, s[6:7] offset:2048 nt
	global_load_dwordx4 v[28:31], v12, s[6:7] offset:3072 nt
	s_add_i32 s2, s2, s4
	s_add_u32 s6, s6, s8
	s_addc_u32 s7, s7, s9
	s_waitcnt vmcnt(0)
	v_cvt_f32_f16_e32 v36, v16
	v_cvt_f32_f16_sdwa v37, v16 dst_sel:DWORD dst_unused:UNUSED_PAD src0_sel:WORD_1
	v_cvt_f32_f16_e32 v16, v17
	v_cvt_f32_f16_sdwa v17, v17 dst_sel:DWORD dst_unused:UNUSED_PAD src0_sel:WORD_1
	v_cvt_f32_f16_e32 v38, v18
	v_cvt_f32_f16_sdwa v39, v18 dst_sel:DWORD dst_unused:UNUSED_PAD src0_sel:WORD_1
	v_cvt_f32_f16_e32 v40, v19
	v_cvt_f32_f16_sdwa v41, v19 dst_sel:DWORD dst_unused:UNUSED_PAD src0_sel:WORD_1
	v_cvt_f32_f16_e32 v42, v20
	v_cvt_f32_f16_sdwa v43, v20 dst_sel:DWORD dst_unused:UNUSED_PAD src0_sel:WORD_1
	v_cvt_f32_f16_e32 v20, v21
	v_cvt_f32_f16_sdwa v21, v21 dst_sel:DWORD dst_unused:UNUSED_PAD src0_sel:WORD_1
	v_cvt_f32_f16_e32 v44, v22
	v_cvt_f32_f16_sdwa v45, v22 dst_sel:DWORD dst_unused:UNUSED_PAD src0_sel:WORD_1
	v_cvt_f32_f16_e32 v22, v23
	v_cvt_f32_f16_sdwa v23, v23 dst_sel:DWORD dst_unused:UNUSED_PAD src0_sel:WORD_1
	v_cvt_f32_f16_e32 v46, v24
	v_cvt_f32_f16_sdwa v47, v24 dst_sel:DWORD dst_unused:UNUSED_PAD src0_sel:WORD_1
	v_cvt_f32_f16_e32 v24, v25
	v_cvt_f32_f16_sdwa v25, v25 dst_sel:DWORD dst_unused:UNUSED_PAD src0_sel:WORD_1
	v_cvt_f32_f16_e32 v48, v26
	v_cvt_f32_f16_sdwa v49, v26 dst_sel:DWORD dst_unused:UNUSED_PAD src0_sel:WORD_1
	v_cvt_f32_f16_e32 v26, v27
	v_cvt_f32_f16_sdwa v27, v27 dst_sel:DWORD dst_unused:UNUSED_PAD src0_sel:WORD_1
	v_pk_mul_f32 v[18:19], v[36:37], v[36:37]
	v_pk_mul_f32 v[54:55], v[16:17], v[16:17]
	v_pk_mul_f32 v[56:57], v[38:39], v[38:39]
	v_pk_mul_f32 v[58:59], v[40:41], v[40:41]
	v_cvt_f32_f16_e32 v50, v28
	v_cvt_f32_f16_sdwa v51, v28 dst_sel:DWORD dst_unused:UNUSED_PAD src0_sel:WORD_1
	v_cvt_f32_f16_e32 v28, v29
	v_cvt_f32_f16_sdwa v29, v29 dst_sel:DWORD dst_unused:UNUSED_PAD src0_sel:WORD_1
	v_pk_mul_f32 v[60:61], v[42:43], v[42:43]
	v_pk_mul_f32 v[62:63], v[20:21], v[20:21]
	v_add_f32_e32 v15, v58, v59
	v_add_f32_e32 v56, v56, v57
	v_add_f32_e32 v54, v54, v55
	v_add_f32_e32 v18, v18, v19
	v_cvt_f32_f16_e32 v52, v30
	v_cvt_f32_f16_sdwa v53, v30 dst_sel:DWORD dst_unused:UNUSED_PAD src0_sel:WORD_1
	v_cvt_f32_f16_e32 v30, v31
	v_cvt_f32_f16_sdwa v31, v31 dst_sel:DWORD dst_unused:UNUSED_PAD src0_sel:WORD_1
	v_pk_mul_f32 v[64:65], v[44:45], v[44:45]
	v_pk_mul_f32 v[66:67], v[22:23], v[22:23]
	v_add_f32_e32 v19, v62, v63
	v_add_f32_e32 v55, v60, v61
	v_add_f32_e32 v15, v56, v15
	v_add_f32_e32 v18, v18, v54
	v_pk_mul_f32 v[68:69], v[46:47], v[46:47]
	v_pk_mul_f32 v[70:71], v[24:25], v[24:25]
	v_add_f32_e32 v57, v66, v67
	v_add_f32_e32 v58, v64, v65
	v_add_f32_e32 v19, v55, v19
	v_add_f32_e32 v15, v18, v15
	v_pk_mul_f32 v[72:73], v[48:49], v[48:49]
	v_pk_mul_f32 v[74:75], v[26:27], v[26:27]
	v_add_f32_e32 v59, v70, v71
	v_add_f32_e32 v60, v68, v69
	v_add_f32_e32 v54, v58, v57
	v_add_f32_e32 v15, v15, v19
	v_pk_mul_f32 v[76:77], v[50:51], v[50:51]
	v_pk_mul_f32 v[78:79], v[28:29], v[28:29]
	v_add_f32_e32 v61, v74, v75
	v_add_f32_e32 v62, v72, v73
	v_add_f32_e32 v55, v60, v59
	v_add_f32_e32 v15, v15, v54
	v_pk_mul_f32 v[80:81], v[52:53], v[52:53]
	v_pk_mul_f32 v[82:83], v[30:31], v[30:31]
	v_add_f32_e32 v63, v78, v79
	v_add_f32_e32 v64, v76, v77
	v_add_f32_e32 v56, v62, v61
	v_add_f32_e32 v15, v15, v55
	v_add_f32_e32 v65, v82, v83
	v_add_f32_e32 v66, v80, v81
	v_add_f32_e32 v57, v64, v63
	v_add_f32_e32 v15, v15, v56
	v_add_f32_e32 v58, v66, v65
	v_add_f32_e32 v15, v15, v57
	v_add_f32_e32 v15, v15, v58
	ds_swizzle_b32 v18, v15 offset:swizzle(SWAP,1)
	s_waitcnt lgkmcnt(0)
	v_add_f32_e32 v15, v15, v18
	ds_swizzle_b32 v18, v15 offset:swizzle(SWAP,2)
	s_waitcnt lgkmcnt(0)
	v_add_f32_e32 v15, v15, v18
	ds_swizzle_b32 v18, v15 offset:swizzle(SWAP,4)
	s_waitcnt lgkmcnt(0)
	v_add_f32_e32 v15, v15, v18
	ds_swizzle_b32 v18, v15 offset:swizzle(SWAP,8)
	s_waitcnt lgkmcnt(0)
	v_add_f32_e32 v15, v15, v18
	ds_swizzle_b32 v18, v15 offset:swizzle(SWAP,16)
	s_waitcnt lgkmcnt(0)
	v_add_f32_e32 v15, v15, v18
	v_mov_b32_e32 v18, v15
	s_nop 1
	v_permlane32_swap_b32_e32 v15, v18
	v_add_f32_e32 v15, v15, v18
	v_fmamk_f32 v15, v15, 0x3a000000, v13
	v_mul_f32_e32 v18, 0x4f800000, v15
	v_cmp_gt_f32_e32 vcc, s3, v15
	s_nop 1
	v_cndmask_b32_e32 v15, v15, v18, vcc
	v_sqrt_f32_e32 v18, v15
	s_nop 0
	v_add_u32_e32 v19, -1, v18
	v_add_u32_e32 v54, 1, v18
	v_fma_f32 v55, -v19, v18, v15
	v_fma_f32 v56, -v54, v18, v15
	v_cmp_ge_f32_e64 s[0:1], 0, v55
	s_nop 1
	v_cndmask_b32_e64 v18, v18, v19, s[0:1]
	v_cmp_lt_f32_e64 s[0:1], 0, v56
	s_nop 1
	v_cndmask_b32_e64 v18, v18, v54, s[0:1]
	v_mul_f32_e32 v19, 0x37800000, v18
	v_cndmask_b32_e32 v18, v18, v19, vcc
	v_cmp_class_f32_e32 vcc, v15, v14
	s_nop 1
	v_cndmask_b32_e32 v15, v18, v15, vcc
	v_div_scale_f32 v18, s[0:1], v15, v15, 1.0
	v_rcp_f32_e32 v54, v18
	v_div_scale_f32 v19, vcc, 1.0, v15, 1.0
	v_fma_f32 v55, -v18, v54, 1.0
	v_fmac_f32_e32 v54, v55, v54
	v_mul_f32_e32 v55, v19, v54
	v_fma_f32 v56, -v18, v55, v19
	v_fmac_f32_e32 v55, v56, v54
	v_fma_f32 v18, -v18, v55, v19
	v_div_fmas_f32 v18, v18, v54, v55
	v_div_fixup_f32 v54, v18, v15, 1.0
	v_pk_mul_f32 v[36:37], v[54:55], v[36:37] op_sel_hi:[0,1]
	v_pk_mul_f32 v[16:17], v[54:55], v[16:17] op_sel_hi:[0,1]
	v_pk_mul_f32 v[18:19], v[16:17], v[86:87]
	v_pk_mul_f32 v[16:17], v[36:37], v[84:85]
	global_store_dwordx4 v0, v[16:19], s[10:11]
	v_pk_mul_f32 v[32:33], v[54:55], v[40:41] op_sel_hi:[0,1]
	v_pk_mul_f32 v[34:35], v[54:55], v[38:39] op_sel_hi:[0,1]
	v_pk_mul_f32 v[20:21], v[54:55], v[20:21] op_sel_hi:[0,1]
	s_nop 1
	v_pk_mul_f32 v[16:17], v[34:35], v[88:89]
	v_pk_mul_f32 v[18:19], v[32:33], v[90:91]
	global_store_dwordx4 v0, v[16:19], s[10:11] offset:16
	v_pk_mul_f32 v[32:33], v[54:55], v[42:43] op_sel_hi:[0,1]
	s_nop 1
	v_pk_mul_f32 v[16:17], v[32:33], v[92:93]
	v_pk_mul_f32 v[18:19], v[20:21], v[94:95]
	global_store_dwordx4 v0, v[16:19], s[10:11] offset:2048
	v_pk_mul_f32 v[20:21], v[54:55], v[22:23] op_sel_hi:[0,1]
	v_pk_mul_f32 v[22:23], v[54:55], v[44:45] op_sel_hi:[0,1]
	s_nop 1
	v_pk_mul_f32 v[16:17], v[22:23], v[96:97]
	v_pk_mul_f32 v[18:19], v[20:21], v[98:99]
	global_store_dwordx4 v0, v[16:19], s[10:11] offset:2064
	v_lshl_add_u64 v[20:21], s[10:11], 0, v[0:1]
	v_add_co_u32_e32 v20, vcc, s5, v20
	v_pk_mul_f32 v[22:23], v[54:55], v[24:25] op_sel_hi:[0,1]
	v_pk_mul_f32 v[24:25], v[54:55], v[46:47] op_sel_hi:[0,1]
	v_addc_co_u32_e32 v21, vcc, 0, v21, vcc
	s_add_u32 s10, s10, s12
	s_addc_u32 s11, s11, s13
	s_cmpk_gt_i32 s2, 0x7fff
	s_nop 1
	v_pk_mul_f32 v[16:17], v[24:25], v[100:101]
	v_pk_mul_f32 v[18:19], v[22:23], v[102:103]
	global_store_dwordx4 v[20:21], v[16:19], off
	v_pk_mul_f32 v[22:23], v[54:55], v[26:27] op_sel_hi:[0,1]
	v_pk_mul_f32 v[24:25], v[54:55], v[48:49] op_sel_hi:[0,1]
	s_nop 1
	v_pk_mul_f32 v[16:17], v[24:25], v[104:105]
	v_pk_mul_f32 v[18:19], v[22:23], v[106:107]
	global_store_dwordx4 v[20:21], v[16:19], off offset:16
	v_pk_mul_f32 v[22:23], v[54:55], v[28:29] op_sel_hi:[0,1]
	v_pk_mul_f32 v[24:25], v[54:55], v[50:51] op_sel_hi:[0,1]
	s_nop 1
	v_pk_mul_f32 v[16:17], v[24:25], v[108:109]
	v_pk_mul_f32 v[18:19], v[22:23], v[110:111]
	global_store_dwordx4 v[20:21], v[16:19], off offset:2048
	v_pk_mul_f32 v[22:23], v[54:55], v[30:31] op_sel_hi:[0,1]
	v_pk_mul_f32 v[24:25], v[54:55], v[52:53] op_sel_hi:[0,1]
	s_nop 1
	v_pk_mul_f32 v[16:17], v[24:25], v[112:113]
	v_pk_mul_f32 v[18:19], v[22:23], v[114:115]
	global_store_dwordx4 v[20:21], v[16:19], off offset:2064
	s_cbranch_scc0 .LBB0_978
